# k_point: kernargs loaded once up front, in-branch vmcnt(0) removed, gelu repacked (bit-identical) with 2-way interleave instead of s_nop padding
# baseline (speedup 1.0000x reference)
_Z7k_pointPDF16_S_S_PKfS1_S1_S1_S1_S1_S1_S1_S1_S1_S1_S1_S1_S1_:
	v_bfe_u32 v105, v0, 6, 2
	v_lshrrev_b32_e32 v104, 8, v0
	v_lshlrev_b32_e32 v1, 4, v105
	s_load_dwordx16 s[60:75], s[0:1], 0x0
	s_load_dwordx16 s[76:91], s[0:1], 0x40
	s_load_dwordx2 s[92:93], s[0:1], 0x80
	v_lshl_or_b32 v14, s2, 6, v1
	v_lshlrev_b32_e32 v107, 3, v104
	v_or_b32_e32 v2, v14, v107
	v_lshlrev_b32_e32 v2, 6, v2
	v_ashrrev_i32_e32 v3, 31, v2
	v_and_b32_e32 v103, 63, v0
	v_lshlrev_b64 v[2:3], 2, v[2:3]
	s_waitcnt lgkmcnt(0)
	v_lshl_add_u64 v[4:5], s[68:69], 0, v[2:3]
	v_lshlrev_b32_e32 v94, 4, v103
	v_mov_b32_e32 v95, 0
	v_lshl_add_u64 v[4:5], v[4:5], 0, v[94:95]
	v_lshl_add_u64 v[2:3], s[70:71], 0, v[2:3]
	v_mul_u32_u24_e32 v113, 0xe39, v0
	s_movk_i32 s2, 0xffee
	v_lshl_add_u64 v[2:3], v[2:3], 0, v[94:95]
	global_load_dwordx4 v[58:61], v[4:5], off nt
	global_load_dwordx4 v[50:53], v[4:5], off offset:1024 nt
	global_load_dwordx4 v[62:65], v[2:3], off nt
	global_load_dwordx4 v[54:57], v[2:3], off offset:1024 nt
	v_mul_i32_i24_sdwa v4, v113, s2 dst_sel:DWORD dst_unused:UNUSED_PAD src0_sel:WORD_1 src1_sel:DWORD
	s_movk_i32 s3, 0x48
	v_mul_u32_u24_sdwa v2, v113, s3 dst_sel:DWORD dst_unused:UNUSED_PAD src0_sel:WORD_1 src1_sel:DWORD
	v_add_lshl_u32 v96, v4, v0, 2
	v_lshlrev_b32_e32 v2, 2, v2
	v_mov_b32_e32 v3, v95
	v_ashrrev_i32_e32 v97, 31, v96
	v_lshl_add_u64 v[6:7], s[74:75], 0, v[2:3]
	v_lshlrev_b64 v[4:5], 2, v[96:97]
	v_or_b32_e32 v8, 0x200, v0
	v_lshl_add_u64 v[10:11], v[6:7], 0, v[4:5]
	v_mul_u32_u24_e32 v6, 0xe39, v8
	v_mul_i32_i24_sdwa v9, v6, s2 dst_sel:DWORD dst_unused:UNUSED_PAD src0_sel:WORD_1 src1_sel:DWORD
	v_mul_u32_u24_sdwa v6, v6, s3 dst_sel:DWORD dst_unused:UNUSED_PAD src0_sel:WORD_1 src1_sel:DWORD
	v_add_lshl_u32 v8, v9, v8, 2
	v_lshlrev_b32_e32 v6, 2, v6
	v_mov_b32_e32 v7, v95
	v_ashrrev_i32_e32 v9, 31, v8
	v_lshl_add_u64 v[12:13], s[74:75], 0, v[6:7]
	v_lshlrev_b64 v[8:9], 2, v[8:9]
	v_lshl_add_u64 v[12:13], v[12:13], 0, v[8:9]
	v_or_b32_e32 v106, 0x400, v0
	global_load_dwordx4 v[90:93], v[10:11], off
	global_load_dwordx4 v[86:89], v[12:13], off
	v_min_u32_e32 v12, 0x50f, v106
	v_mul_u32_u24_e32 v15, 0xe39, v12
	v_mul_i32_i24_sdwa v13, v15, s2 dst_sel:DWORD dst_unused:UNUSED_PAD src0_sel:WORD_1 src1_sel:DWORD
	v_mul_u32_u24_sdwa v10, v15, s3 dst_sel:DWORD dst_unused:UNUSED_PAD src0_sel:WORD_1 src1_sel:DWORD
	v_add_lshl_u32 v12, v13, v12, 2
	v_lshlrev_b32_e32 v98, 2, v10
	v_mov_b32_e32 v99, v95
	v_ashrrev_i32_e32 v13, 31, v12
	v_lshl_add_u64 v[10:11], s[74:75], 0, v[98:99]
	v_lshlrev_b64 v[100:101], 2, v[12:13]
	v_lshl_add_u64 v[10:11], v[10:11], 0, v[100:101]
	s_movk_i32 s2, 0x42
	global_load_dwordx4 v[82:85], v[10:11], off
	v_lshl_add_u64 v[10:11], s[78:79], 0, v[2:3]
	v_min_u32_sdwa v3, v15, s2 dst_sel:DWORD dst_unused:UNUSED_PAD src0_sel:WORD_1 src1_sel:DWORD
	v_lshl_add_u64 v[10:11], v[10:11], 0, v[4:5]
	v_lshl_add_u64 v[12:13], s[78:79], 0, v[6:7]
	v_mul_u32_u24_e32 v3, 0x48, v3
	v_lshl_add_u64 v[12:13], v[12:13], 0, v[8:9]
	global_load_dwordx4 v[74:77], v[10:11], off
	global_load_dwordx4 v[78:81], v[12:13], off
	v_lshlrev_b32_e32 v10, 2, v3
	v_mov_b32_e32 v11, v95
	v_lshl_add_u64 v[10:11], s[78:79], 0, v[10:11]
	v_min_u32_e32 v3, 0x47, v0
	v_lshl_add_u64 v[10:11], v[10:11], 0, v[100:101]
	v_lshlrev_b32_e32 v3, 2, v3
	global_load_dwordx4 v[70:73], v[10:11], off
	global_load_dword v109, v3, s[76:77]
	global_load_dword v110, v3, s[80:81]
	global_load_dword v111, v3, s[84:85]
	global_load_dword v112, v3, s[90:91]
	s_movk_i32 s2, 0x100
	v_and_b32_e32 v102, 15, v0
	v_cmp_gt_u32_e32 vcc, s2, v0
	s_movk_i32 s2, 0xff
	v_or_b32_e32 v97, v14, v102
	v_cmp_lt_u32_e64 s[4:5], s2, v0
	s_and_saveexec_b64 s[2:3], s[4:5]
	s_xor_b64 s[6:7], exec, s[2:3]
	s_cbranch_execz .LBB0_2
	v_lshl_add_u32 v10, v97, 1, v97
	v_ashrrev_i32_e32 v11, 31, v10
	v_mov_b32_e32 v69, v95
	v_lshl_add_u64 v[10:11], v[10:11], 2, s[66:67]
	global_load_dwordx3 v[66:68], v[10:11], off nt
.LBB0_2:
	s_or_saveexec_b64 s[14:15], s[6:7]
	v_bfe_u32 v95, v0, 4, 2
	v_lshlrev_b32_e32 v108, 4, v95
	s_xor_b64 exec, exec, s[14:15]
	s_cbranch_execz .LBB0_4
	v_lshlrev_b32_e32 v10, 3, v97
	v_ashrrev_i32_e32 v11, 31, v10
	v_and_b32_e32 v12, 16, v108
	v_mov_b32_e32 v13, 0
	v_lshl_add_u64 v[10:11], v[10:11], 2, s[72:73]
	v_lshl_add_u64 v[10:11], v[10:11], 0, v[12:13]
	global_load_dwordx4 v[66:69], v[10:11], off nt
.LBB0_4:
	s_or_b64 exec, exec, s[14:15]
	v_mov_b32_e32 v3, 0
	v_lshl_add_u64 v[10:11], s[82:83], 0, v[2:3]
	v_mov_b32_e32 v7, v3
	v_lshl_add_u64 v[10:11], v[10:11], 0, v[4:5]
	v_lshl_add_u64 v[12:13], s[82:83], 0, v[6:7]
	v_mov_b32_e32 v99, v3
	v_lshl_add_u64 v[12:13], v[12:13], 0, v[8:9]
	global_load_dwordx4 v[46:49], v[10:11], off
	global_load_dwordx4 v[42:45], v[12:13], off
	v_lshl_add_u64 v[10:11], s[82:83], 0, v[98:99]
	v_lshl_add_u64 v[10:11], v[10:11], 0, v[100:101]
	global_load_dwordx4 v[38:41], v[10:11], off
	v_lshl_add_u64 v[10:11], s[88:89], 0, v[2:3]
	v_lshl_add_u64 v[10:11], v[10:11], 0, v[4:5]
	v_lshl_add_u64 v[12:13], s[88:89], 0, v[6:7]
	v_lshl_add_u64 v[12:13], v[12:13], 0, v[8:9]
	global_load_dwordx4 v[34:37], v[10:11], off
	global_load_dwordx4 v[30:33], v[12:13], off
	v_lshl_add_u64 v[10:11], s[88:89], 0, v[98:99]
	v_lshl_add_u64 v[10:11], v[10:11], 0, v[100:101]
	global_load_dwordx4 v[26:29], v[10:11], off
	v_lshl_add_u64 v[10:11], s[86:87], 0, v[2:3]
	v_lshl_add_u64 v[10:11], v[10:11], 0, v[4:5]
	v_lshl_add_u64 v[12:13], s[86:87], 0, v[6:7]
	v_lshl_add_u64 v[12:13], v[12:13], 0, v[8:9]
	global_load_dwordx4 v[22:25], v[10:11], off
	global_load_dwordx4 v[18:21], v[12:13], off
	v_lshl_add_u64 v[10:11], s[86:87], 0, v[98:99]
	v_lshl_add_u64 v[2:3], s[92:93], 0, v[2:3]
	v_lshl_add_u64 v[10:11], v[10:11], 0, v[100:101]
	v_lshl_add_u64 v[2:3], v[2:3], 0, v[4:5]
	v_lshl_add_u64 v[4:5], s[92:93], 0, v[6:7]
	global_load_dwordx4 v[14:17], v[10:11], off
	v_lshl_add_u64 v[4:5], v[4:5], 0, v[8:9]
	global_load_dwordx4 v[10:13], v[2:3], off
	global_load_dwordx4 v[6:9], v[4:5], off
	v_lshl_add_u64 v[2:3], s[92:93], 0, v[98:99]
	v_lshl_add_u64 v[2:3], v[2:3], 0, v[100:101]
	global_load_dwordx4 v[2:5], v[2:3], off
	s_movk_i32 s2, 0x50
	s_waitcnt vmcnt(21)
	v_cvt_pk_f16_f32 v93, v92, v93
	v_cvt_pk_f16_f32 v92, v90, v91
	v_mul_u32_u24_sdwa v90, v113, s2 dst_sel:DWORD dst_unused:UNUSED_PAD src0_sel:WORD_1 src1_sel:DWORD
	v_lshlrev_b32_e32 v90, 1, v90
	v_lshlrev_b32_e32 v91, 1, v96
	v_add3_u32 v90, 0, v90, v91
	v_or_b32_e32 v91, 0x200, v0
	v_mul_u32_u24_e32 v96, 0xe39, v91
	s_movk_i32 s8, 0xffee
	ds_write_b64 v90, v[92:93]
	v_mul_i32_i24_sdwa v98, v96, s8 dst_sel:DWORD dst_unused:UNUSED_PAD src0_sel:WORD_1 src1_sel:DWORD
	s_waitcnt vmcnt(20)
	v_cvt_pk_f16_f32 v92, v86, v87
	v_mul_u32_u24_sdwa v86, v96, s2 dst_sel:DWORD dst_unused:UNUSED_PAD src0_sel:WORD_1 src1_sel:DWORD
	v_lshlrev_b32_e32 v86, 1, v86
	v_add_lshl_u32 v87, v98, v91, 3
	s_movk_i32 s2, 0x510
	v_cvt_pk_f16_f32 v93, v88, v89
	v_add3_u32 v89, 0, v86, v87
	v_cmp_gt_u32_e64 s[2:3], s2, v106
	ds_write_b64 v89, v[92:93]
	s_and_saveexec_b64 s[6:7], s[2:3]
	s_cbranch_execz .LBB0_6
	v_mul_u32_u24_e32 v86, 0xe39, v106
	v_mul_i32_i24_sdwa v87, v86, s8 dst_sel:DWORD dst_unused:UNUSED_PAD src0_sel:WORD_1 src1_sel:DWORD
	s_movk_i32 s8, 0xa0
	s_waitcnt vmcnt(19)
	v_cvt_pk_f16_f32 v85, v84, v85
	v_cvt_pk_f16_f32 v84, v82, v83
	v_mul_u32_u24_sdwa v82, v86, s8 dst_sel:DWORD dst_unused:UNUSED_PAD src0_sel:WORD_1 src1_sel:DWORD
	v_add_lshl_u32 v83, v87, v106, 3
	v_add3_u32 v82, 0, v82, v83
	ds_write_b64 v82, v[84:85]

.LBB0_10:
	s_or_b64 exec, exec, s[8:9]
	s_waitcnt vmcnt(16)
	v_add_u32_e32 v70, v1, v107
	v_pk_add_f32 v[60:61], v[60:61], v[64:65]
	v_pk_add_f32 v[58:59], v[58:59], v[62:63]
	v_cvt_pk_f16_f32 v61, v60, v61
	v_cvt_pk_f16_f32 v60, v58, v59
	v_or_b32_e32 v58, v95, v70
	v_pk_add_f32 v[52:53], v[52:53], v[56:57]
	v_pk_add_f32 v[50:51], v[50:51], v[54:55]
	v_or_b32_e32 v1, v1, v102
	v_lshlrev_b32_e32 v71, 3, v102
	s_add_i32 s6, 0, 0x14300
	v_mul_u32_u24_e32 v58, 0x88, v58
	v_cvt_pk_f16_f32 v53, v52, v53
	v_cvt_pk_f16_f32 v52, v50, v51
	v_mul_u32_u24_e32 v1, 0x88, v1
	v_lshlrev_b32_e32 v50, 3, v95
	v_lshlrev_b32_e32 v93, 2, v95
	v_add3_u32 v58, s6, v71, v58
	v_add3_u32 v1, s6, v1, v50
	v_lshrrev_b32_e32 v50, 2, v102
	v_and_b32_e32 v87, 4, v93
	ds_write2_b64 v58, v[60:61], v[52:53] offset1:68
	v_or_b32_e32 v52, v87, v50
	v_or_b32_e32 v50, v93, v50
	s_movk_i32 s6, 0x2d00
	v_lshlrev_b32_e32 v95, 2, v102
	v_mul_u32_u24_e32 v50, 0x50, v50
	s_waitcnt lgkmcnt(0)
	s_barrier
	ds_read2_b64 v[54:57], v1 offset1:4
	ds_read2_b64 v[62:65], v1 offset0:8 offset1:12
	v_mad_u32_u24 v86, v104, s6, 0
	v_and_b32_e32 v51, 12, v95
	v_lshlrev_b32_e32 v88, 1, v50
	v_mul_u32_u24_e32 v91, 0x50, v52
	v_lshlrev_b32_e32 v92, 1, v51
	v_add_u32_e32 v121, v86, v88
	v_mul_u32_u24_e32 v1, 0x140, v104
	s_add_i32 s11, 0, 0x10e00
	v_lshl_add_u32 v96, v91, 1, v86
	v_add_u32_e32 v100, v121, v92
	v_cndmask_b32_e64 v122, 32, 16, s[4:5]
	v_cmp_gt_u32_e64 s[20:21], v122, v103
	s_waitcnt vmcnt(12)
	s_nop 1
	v_cndmask_b32_e64 v66, 0, v66, s[20:21]
	v_cndmask_b32_e64 v67, 0, v67, s[20:21]
	v_cndmask_b32_e64 v68, 0, v68, s[20:21]
	v_cndmask_b32_e64 v69, 0, v69, s[20:21]
	v_cvt_pk_f16_f32 v66, v66, v67
	v_cvt_pk_f16_f32 v67, v68, v69
	v_add3_u32 v1, s11, v1, v108
	v_add_u32_e32 v107, v96, v92
	v_add3_u32 v120, v86, v92, v88
	ds_read_b64_tr_b16 v[52:53], v100 offset:2560
	ds_read_b64_tr_b16 v[50:51], v120
	ds_read_b64_tr_b16 v[58:59], v120 offset:32
	ds_read_b64_tr_b16 v[68:69], v120 offset:5120
	ds_read_b64_tr_b16 v[70:71], v100 offset:7680
	ds_read_b128 v[72:75], v1
	ds_read_b128 v[76:79], v1 offset:64
	ds_read_b64_tr_b16 v[80:81], v120 offset:5152
	ds_read_b64_tr_b16 v[98:99], v120 offset:5248
	s_waitcnt vmcnt(15)
	ds_read_b64_tr_b16 v[108:109], v120 offset:64
	s_waitcnt vmcnt(12)
	ds_read_b64_tr_b16 v[112:113], v120 offset:5184
	s_waitcnt lgkmcnt(5)
	v_mfma_f32_16x16x32_f16 v[72:75], v[50:53], v[54:57], v[72:75]
	ds_read_b64_tr_b16 v[50:51], v107 offset:10240
	v_mov_b32_e32 v52, 0
	v_mov_b32_e32 v53, v52
	ds_read_b64_tr_b16 v[60:61], v100 offset:2592
	ds_read_b64_tr_b16 v[84:85], v100 offset:2688
	v_mfma_f32_16x16x32_f16 v[70:73], v[68:71], v[62:65], v[72:75]
	v_mov_b32_e32 v68, v52
	v_mov_b32_e32 v69, v52
	ds_read_b128 v[116:119], v1 offset:256
	s_waitcnt lgkmcnt(2)
	v_mfma_f32_16x16x32_f16 v[58:61], v[58:61], v[54:57], v[76:79]
	s_mov_b32 s7, 0x3fb504f3
	s_mov_b32 s9, 0x3ea7ba05
	s_mov_b32 s8, 0xbfba00e3
	v_mfma_f32_16x16x32_f16 v[70:73], v[50:53], v[66:69], v[70:73]
	ds_read_b64_tr_b16 v[82:83], v100 offset:7712
	ds_read_b64_tr_b16 v[110:111], v100 offset:2624
	ds_read_b64_tr_b16 v[50:51], v107 offset:10304
	v_mov_b32_e32 v76, v52
	v_mov_b32_e32 v77, v52
	s_waitcnt lgkmcnt(2)
	v_mfma_f32_16x16x32_f16 v[58:61], v[80:83], v[62:65], v[58:61]
	ds_read_b64_tr_b16 v[74:75], v107 offset:10272
	ds_read_b64_tr_b16 v[114:115], v100 offset:7744
	ds_read_b64_tr_b16 v[100:101], v100 offset:7808
	s_mov_b32 s6, 0x3f87dc22
	s_mov_b32 s10, 0xbe91a98e
	s_waitcnt lgkmcnt(2)
	v_mfma_f32_16x16x32_f16 v[74:77], v[74:77], v[66:69], v[58:61]
	s_nop 2
	ds_read_b128 v[58:61], v1 offset:128
	ds_read_b128 v[78:81], v1 offset:192
	v_or_b32_e32 v1, 48, v95
	v_lshlrev_b32_e32 v95, 1, v1
	v_add3_u32 v1, v86, v95, v88
	s_waitcnt lgkmcnt(1)
	v_mfma_f32_16x16x32_f16 v[58:61], v[108:111], v[54:57], v[58:61]
	ds_read_b64_tr_b16 v[108:109], v1
	ds_read_b64_tr_b16 v[82:83], v120 offset:128
	v_add_u32_e32 v120, v121, v95
	ds_read_b64_tr_b16 v[110:111], v120 offset:2560
	v_mfma_f32_16x16x32_f16 v[58:61], v[112:115], v[62:65], v[58:61]
	s_mov_b32 s12, 0x3e827906
	v_mfma_f32_16x16x32_f16 v[112:115], v[50:53], v[66:69], v[58:61]
	s_nop 5
	ds_read_b64_tr_b16 v[60:61], v120 offset:7680
	ds_read_b64_tr_b16 v[58:59], v1 offset:5120
	v_add_u32_e32 v1, v96, v95
	ds_read_b64_tr_b16 v[50:51], v1 offset:10240
	s_waitcnt lgkmcnt(3)
	v_mfma_f32_16x16x32_f16 v[78:81], v[108:111], v[54:57], v[78:81]
	s_waitcnt lgkmcnt(1)
	v_mfma_f32_16x16x32_f16 v[58:61], v[58:61], v[62:65], v[78:81]
	s_waitcnt lgkmcnt(0)
	v_mfma_f32_16x16x32_f16 v[58:61], v[50:53], v[66:69], v[58:61]
	ds_read_b64_tr_b16 v[50:51], v107 offset:10368
	v_mfma_f32_16x16x32_f16 v[54:57], v[82:85], v[54:57], v[116:119]
	v_mfma_f32_16x16x32_f16 v[54:57], v[98:101], v[62:65], v[54:57]
	s_waitcnt lgkmcnt(0)
	v_mfma_f32_16x16x32_f16 v[54:57], v[50:53], v[66:69], v[54:57]
	s_mov_b32 s24, 0x3fb504f3
	s_mov_b32 s26, 0x3ea7ba05
	s_mov_b32 s28, 0xbfb8aa3b
	s_mov_b32 s30, 0x3f87dc22
	s_mov_b32 s32, 0xbfba00e3
	s_mov_b32 s34, 0x3fb5f0e3
	s_mov_b32 s36, 0xbe91a98e
	s_mov_b32 s38, 0x3e827906
	v_mov_b32_e32 v152, s32
	v_mov_b32_e32 v153, s32
	v_pk_mul_f32 v[124:125], v[70:71], 0.5 op_sel_hi:[1,0]
	v_pk_mul_f32 v[138:139], v[72:73], 0.5 op_sel_hi:[1,0]
	v_and_b32_e32 v126, 0x7fffffff, v124
	v_and_b32_e32 v140, 0x7fffffff, v138
	v_and_b32_e32 v127, 0x7fffffff, v125
	v_and_b32_e32 v141, 0x7fffffff, v139
	v_pk_mul_f32 v[128:129], v[126:127], s[24:25] op_sel_hi:[1,0]
	v_pk_mul_f32 v[142:143], v[140:141], s[24:25] op_sel_hi:[1,0]
	v_pk_fma_f32 v[130:131], v[128:129], s[26:27], 1.0 op_sel_hi:[1,0,0]
	v_pk_fma_f32 v[144:145], v[142:143], s[26:27], 1.0 op_sel_hi:[1,0,0]
	v_pk_mul_f32 v[132:133], v[128:129], s[28:29] op_sel_hi:[1,0]
	v_pk_mul_f32 v[146:147], v[142:143], s[28:29] op_sel_hi:[1,0]
	v_rcp_f32_e32 v130, v130
	v_rcp_f32_e32 v144, v144
	v_rcp_f32_e32 v131, v131
	v_rcp_f32_e32 v145, v145
	v_pk_mul_f32 v[132:133], v[128:129], v[132:133]
	v_pk_mul_f32 v[146:147], v[142:143], v[146:147]
	v_exp_f32_e32 v132, v132
	v_exp_f32_e32 v146, v146
	v_exp_f32_e32 v133, v133
	v_exp_f32_e32 v147, v147
	v_pk_fma_f32 v[134:135], v[130:131], s[30:31], v[152:153] op_sel_hi:[1,0,0]
	v_pk_fma_f32 v[148:149], v[144:145], s[30:31], v[152:153] op_sel_hi:[1,0,0]
	v_pk_fma_f32 v[134:135], v[134:135], v[130:131], s[34:35] op_sel_hi:[1,1,0]
	v_pk_fma_f32 v[148:149], v[148:149], v[144:145], s[34:35] op_sel_hi:[1,1,0]
	v_pk_fma_f32 v[134:135], v[134:135], v[130:131], s[36:37] op_sel_hi:[1,1,0]
	v_pk_fma_f32 v[148:149], v[148:149], v[144:145], s[36:37] op_sel_hi:[1,1,0]
	v_pk_fma_f32 v[134:135], v[134:135], v[130:131], s[38:39] op_sel_hi:[1,1,0]
	v_pk_fma_f32 v[148:149], v[148:149], v[144:145], s[38:39] op_sel_hi:[1,1,0]
	v_pk_mul_f32 v[134:135], v[130:131], v[134:135]
	v_pk_mul_f32 v[148:149], v[144:145], v[148:149]
	v_pk_mul_f32 v[134:135], v[132:133], v[134:135]
	v_pk_mul_f32 v[148:149], v[146:147], v[148:149]
	v_pk_fma_f32 v[136:137], v[70:71], 0.5, v[126:127] op_sel_hi:[1,0,1]
	v_pk_fma_f32 v[150:151], v[72:73], 0.5, v[140:141] op_sel_hi:[1,0,1]
	v_pk_fma_f32 v[62:63], v[126:127], v[134:135], v[136:137] neg_lo:[1,0,0] neg_hi:[1,0,0]
	v_pk_fma_f32 v[64:65], v[140:141], v[148:149], v[150:151] neg_lo:[1,0,0] neg_hi:[1,0,0]
	v_pk_mul_f32 v[124:125], v[74:75], 0.5 op_sel_hi:[1,0]
	v_pk_mul_f32 v[138:139], v[76:77], 0.5 op_sel_hi:[1,0]
	v_and_b32_e32 v126, 0x7fffffff, v124
	v_and_b32_e32 v140, 0x7fffffff, v138
	v_and_b32_e32 v127, 0x7fffffff, v125
	v_and_b32_e32 v141, 0x7fffffff, v139
	v_pk_mul_f32 v[128:129], v[126:127], s[24:25] op_sel_hi:[1,0]
	v_pk_mul_f32 v[142:143], v[140:141], s[24:25] op_sel_hi:[1,0]
	v_pk_fma_f32 v[130:131], v[128:129], s[26:27], 1.0 op_sel_hi:[1,0,0]
	v_pk_fma_f32 v[144:145], v[142:143], s[26:27], 1.0 op_sel_hi:[1,0,0]
	v_pk_mul_f32 v[132:133], v[128:129], s[28:29] op_sel_hi:[1,0]
	v_pk_mul_f32 v[146:147], v[142:143], s[28:29] op_sel_hi:[1,0]
	v_rcp_f32_e32 v130, v130
	v_rcp_f32_e32 v144, v144
	v_rcp_f32_e32 v131, v131
	v_rcp_f32_e32 v145, v145
	v_pk_mul_f32 v[132:133], v[128:129], v[132:133]
	v_pk_mul_f32 v[146:147], v[142:143], v[146:147]
	v_exp_f32_e32 v132, v132
	v_exp_f32_e32 v146, v146
	v_exp_f32_e32 v133, v133
	v_exp_f32_e32 v147, v147
	v_pk_fma_f32 v[134:135], v[130:131], s[30:31], v[152:153] op_sel_hi:[1,0,0]
	v_pk_fma_f32 v[148:149], v[144:145], s[30:31], v[152:153] op_sel_hi:[1,0,0]
	v_pk_fma_f32 v[134:135], v[134:135], v[130:131], s[34:35] op_sel_hi:[1,1,0]
	v_pk_fma_f32 v[148:149], v[148:149], v[144:145], s[34:35] op_sel_hi:[1,1,0]
	v_pk_fma_f32 v[134:135], v[134:135], v[130:131], s[36:37] op_sel_hi:[1,1,0]
	v_pk_fma_f32 v[148:149], v[148:149], v[144:145], s[36:37] op_sel_hi:[1,1,0]
	v_pk_fma_f32 v[134:135], v[134:135], v[130:131], s[38:39] op_sel_hi:[1,1,0]
	v_pk_fma_f32 v[148:149], v[148:149], v[144:145], s[38:39] op_sel_hi:[1,1,0]
	v_pk_mul_f32 v[134:135], v[130:131], v[134:135]
	v_pk_mul_f32 v[148:149], v[144:145], v[148:149]
	v_pk_mul_f32 v[134:135], v[132:133], v[134:135]
	v_pk_mul_f32 v[148:149], v[146:147], v[148:149]
	v_pk_fma_f32 v[136:137], v[74:75], 0.5, v[126:127] op_sel_hi:[1,0,1]
	v_pk_fma_f32 v[150:151], v[76:77], 0.5, v[140:141] op_sel_hi:[1,0,1]
	v_pk_fma_f32 v[74:75], v[126:127], v[134:135], v[136:137] neg_lo:[1,0,0] neg_hi:[1,0,0]
	v_pk_fma_f32 v[76:77], v[140:141], v[148:149], v[150:151] neg_lo:[1,0,0] neg_hi:[1,0,0]
	v_pk_mul_f32 v[124:125], v[112:113], 0.5 op_sel_hi:[1,0]
	v_pk_mul_f32 v[138:139], v[114:115], 0.5 op_sel_hi:[1,0]
	v_and_b32_e32 v126, 0x7fffffff, v124
	v_and_b32_e32 v140, 0x7fffffff, v138
	v_and_b32_e32 v127, 0x7fffffff, v125
	v_and_b32_e32 v141, 0x7fffffff, v139
	v_pk_mul_f32 v[128:129], v[126:127], s[24:25] op_sel_hi:[1,0]
	v_pk_mul_f32 v[142:143], v[140:141], s[24:25] op_sel_hi:[1,0]
	v_pk_fma_f32 v[130:131], v[128:129], s[26:27], 1.0 op_sel_hi:[1,0,0]
	v_pk_fma_f32 v[144:145], v[142:143], s[26:27], 1.0 op_sel_hi:[1,0,0]
	v_pk_mul_f32 v[132:133], v[128:129], s[28:29] op_sel_hi:[1,0]
	v_pk_mul_f32 v[146:147], v[142:143], s[28:29] op_sel_hi:[1,0]
	v_rcp_f32_e32 v130, v130
	v_rcp_f32_e32 v144, v144
	v_rcp_f32_e32 v131, v131
	v_rcp_f32_e32 v145, v145
	v_pk_mul_f32 v[132:133], v[128:129], v[132:133]
	v_pk_mul_f32 v[146:147], v[142:143], v[146:147]
	v_exp_f32_e32 v132, v132
	v_exp_f32_e32 v146, v146
	v_exp_f32_e32 v133, v133
	v_exp_f32_e32 v147, v147
	v_pk_fma_f32 v[134:135], v[130:131], s[30:31], v[152:153] op_sel_hi:[1,0,0]
	v_pk_fma_f32 v[148:149], v[144:145], s[30:31], v[152:153] op_sel_hi:[1,0,0]
	v_pk_fma_f32 v[134:135], v[134:135], v[130:131], s[34:35] op_sel_hi:[1,1,0]
	v_pk_fma_f32 v[148:149], v[148:149], v[144:145], s[34:35] op_sel_hi:[1,1,0]
	v_pk_fma_f32 v[134:135], v[134:135], v[130:131], s[36:37] op_sel_hi:[1,1,0]
	v_pk_fma_f32 v[148:149], v[148:149], v[144:145], s[36:37] op_sel_hi:[1,1,0]
	v_pk_fma_f32 v[134:135], v[134:135], v[130:131], s[38:39] op_sel_hi:[1,1,0]
	v_pk_fma_f32 v[148:149], v[148:149], v[144:145], s[38:39] op_sel_hi:[1,1,0]
	v_pk_mul_f32 v[134:135], v[130:131], v[134:135]
	v_pk_mul_f32 v[148:149], v[144:145], v[148:149]
	v_pk_mul_f32 v[134:135], v[132:133], v[134:135]
	v_pk_mul_f32 v[148:149], v[146:147], v[148:149]
	v_pk_fma_f32 v[136:137], v[112:113], 0.5, v[126:127] op_sel_hi:[1,0,1]
	v_pk_fma_f32 v[150:151], v[114:115], 0.5, v[140:141] op_sel_hi:[1,0,1]
	v_pk_fma_f32 v[78:79], v[126:127], v[134:135], v[136:137] neg_lo:[1,0,0] neg_hi:[1,0,0]
	v_pk_fma_f32 v[80:81], v[140:141], v[148:149], v[150:151] neg_lo:[1,0,0] neg_hi:[1,0,0]
	v_pk_mul_f32 v[124:125], v[58:59], 0.5 op_sel_hi:[1,0]
	v_pk_mul_f32 v[138:139], v[60:61], 0.5 op_sel_hi:[1,0]
	v_and_b32_e32 v126, 0x7fffffff, v124
	v_and_b32_e32 v140, 0x7fffffff, v138
	v_and_b32_e32 v127, 0x7fffffff, v125
	v_and_b32_e32 v141, 0x7fffffff, v139
	v_pk_mul_f32 v[128:129], v[126:127], s[24:25] op_sel_hi:[1,0]
	v_pk_mul_f32 v[142:143], v[140:141], s[24:25] op_sel_hi:[1,0]
	v_pk_fma_f32 v[130:131], v[128:129], s[26:27], 1.0 op_sel_hi:[1,0,0]
	v_pk_fma_f32 v[144:145], v[142:143], s[26:27], 1.0 op_sel_hi:[1,0,0]
	v_pk_mul_f32 v[132:133], v[128:129], s[28:29] op_sel_hi:[1,0]
	v_pk_mul_f32 v[146:147], v[142:143], s[28:29] op_sel_hi:[1,0]
	v_rcp_f32_e32 v130, v130
	v_rcp_f32_e32 v144, v144
	v_rcp_f32_e32 v131, v131
	v_rcp_f32_e32 v145, v145
	v_pk_mul_f32 v[132:133], v[128:129], v[132:133]
	v_pk_mul_f32 v[146:147], v[142:143], v[146:147]
	v_exp_f32_e32 v132, v132
	v_exp_f32_e32 v146, v146
	v_exp_f32_e32 v133, v133
	v_exp_f32_e32 v147, v147
	v_pk_fma_f32 v[134:135], v[130:131], s[30:31], v[152:153] op_sel_hi:[1,0,0]
	v_pk_fma_f32 v[148:149], v[144:145], s[30:31], v[152:153] op_sel_hi:[1,0,0]
	v_pk_fma_f32 v[134:135], v[134:135], v[130:131], s[34:35] op_sel_hi:[1,1,0]
	v_pk_fma_f32 v[148:149], v[148:149], v[144:145], s[34:35] op_sel_hi:[1,1,0]
	v_pk_fma_f32 v[134:135], v[134:135], v[130:131], s[36:37] op_sel_hi:[1,1,0]
	v_pk_fma_f32 v[148:149], v[148:149], v[144:145], s[36:37] op_sel_hi:[1,1,0]
	v_pk_fma_f32 v[134:135], v[134:135], v[130:131], s[38:39] op_sel_hi:[1,1,0]
	v_pk_fma_f32 v[148:149], v[148:149], v[144:145], s[38:39] op_sel_hi:[1,1,0]
	v_pk_mul_f32 v[134:135], v[130:131], v[134:135]
	v_pk_mul_f32 v[148:149], v[144:145], v[148:149]
	v_pk_mul_f32 v[134:135], v[132:133], v[134:135]
	v_pk_mul_f32 v[148:149], v[146:147], v[148:149]
	v_pk_fma_f32 v[136:137], v[58:59], 0.5, v[126:127] op_sel_hi:[1,0,1]
	v_pk_fma_f32 v[150:151], v[60:61], 0.5, v[140:141] op_sel_hi:[1,0,1]
	v_pk_fma_f32 v[58:59], v[126:127], v[134:135], v[136:137] neg_lo:[1,0,0] neg_hi:[1,0,0]
	v_pk_fma_f32 v[60:61], v[140:141], v[148:149], v[150:151] neg_lo:[1,0,0] neg_hi:[1,0,0]
	v_pk_mul_f32 v[124:125], v[54:55], 0.5 op_sel_hi:[1,0]
	v_pk_mul_f32 v[138:139], v[56:57], 0.5 op_sel_hi:[1,0]
	v_and_b32_e32 v126, 0x7fffffff, v124
	v_and_b32_e32 v140, 0x7fffffff, v138
	v_and_b32_e32 v127, 0x7fffffff, v125
	v_and_b32_e32 v141, 0x7fffffff, v139
	v_pk_mul_f32 v[128:129], v[126:127], s[24:25] op_sel_hi:[1,0]
	v_pk_mul_f32 v[142:143], v[140:141], s[24:25] op_sel_hi:[1,0]
	v_pk_fma_f32 v[130:131], v[128:129], s[26:27], 1.0 op_sel_hi:[1,0,0]
	v_pk_fma_f32 v[144:145], v[142:143], s[26:27], 1.0 op_sel_hi:[1,0,0]
	v_pk_mul_f32 v[132:133], v[128:129], s[28:29] op_sel_hi:[1,0]
	v_pk_mul_f32 v[146:147], v[142:143], s[28:29] op_sel_hi:[1,0]
	v_rcp_f32_e32 v130, v130
	v_rcp_f32_e32 v144, v144
	v_rcp_f32_e32 v131, v131
	v_rcp_f32_e32 v145, v145
	v_pk_mul_f32 v[132:133], v[128:129], v[132:133]
	v_pk_mul_f32 v[146:147], v[142:143], v[146:147]
	v_exp_f32_e32 v132, v132
	v_exp_f32_e32 v146, v146
	v_exp_f32_e32 v133, v133
	v_exp_f32_e32 v147, v147
	v_pk_fma_f32 v[134:135], v[130:131], s[30:31], v[152:153] op_sel_hi:[1,0,0]
	v_pk_fma_f32 v[148:149], v[144:145], s[30:31], v[152:153] op_sel_hi:[1,0,0]
	v_pk_fma_f32 v[134:135], v[134:135], v[130:131], s[34:35] op_sel_hi:[1,1,0]
	v_pk_fma_f32 v[148:149], v[148:149], v[144:145], s[34:35] op_sel_hi:[1,1,0]
	v_pk_fma_f32 v[134:135], v[134:135], v[130:131], s[36:37] op_sel_hi:[1,1,0]
	v_pk_fma_f32 v[148:149], v[148:149], v[144:145], s[36:37] op_sel_hi:[1,1,0]
	v_pk_fma_f32 v[134:135], v[134:135], v[130:131], s[38:39] op_sel_hi:[1,1,0]
	v_pk_fma_f32 v[148:149], v[148:149], v[144:145], s[38:39] op_sel_hi:[1,1,0]
	v_pk_mul_f32 v[134:135], v[130:131], v[134:135]
	v_pk_mul_f32 v[148:149], v[144:145], v[148:149]
	v_pk_mul_f32 v[134:135], v[132:133], v[134:135]
	v_pk_mul_f32 v[148:149], v[146:147], v[148:149]
	v_pk_fma_f32 v[136:137], v[54:55], 0.5, v[126:127] op_sel_hi:[1,0,1]
	v_pk_fma_f32 v[150:151], v[56:57], 0.5, v[140:141] op_sel_hi:[1,0,1]
	v_pk_fma_f32 v[82:83], v[126:127], v[134:135], v[136:137] neg_lo:[1,0,0] neg_hi:[1,0,0]
	v_pk_fma_f32 v[84:85], v[140:141], v[148:149], v[150:151] neg_lo:[1,0,0] neg_hi:[1,0,0]
	v_cvt_pk_f16_f32 v73, v60, v61
	v_cvt_pk_f16_f32 v71, v80, v81
	v_cvt_pk_f16_f32 v70, v78, v79
	v_cvt_pk_f16_f32 v72, v58, v59
	v_cvt_pk_f16_f32 v69, v76, v77
	v_lshlrev_b32_e32 v50, 1, v93
	v_cvt_pk_f16_f32 v67, v64, v65
	v_cvt_pk_f16_f32 v66, v62, v63
	v_cvt_pk_f16_f32 v68, v74, v75
	s_and_saveexec_b64 s[6:7], s[4:5]
	s_xor_b64 s[6:7], exec, s[6:7]
	s_cbranch_execz .LBB0_14
	s_movk_i32 s10, 0x48
	v_mul_lo_u32 v0, v97, s10
	v_ashrrev_i32_e32 v1, 31, v0
	v_mov_b32_e32 v51, v52
	s_waitcnt lgkmcnt(0)
	v_lshl_add_u64 v[0:1], v[0:1], 1, s[64:65]
	v_lshl_add_u64 v[0:1], v[0:1], 0, v[50:51]
	v_cvt_pk_f16_f32 v55, v64, v65
	v_cvt_pk_f16_f32 v54, v62, v63
	global_store_dwordx2 v[0:1], v[54:55], off
	v_cvt_pk_f16_f32 v55, v76, v77
	v_cvt_pk_f16_f32 v54, v74, v75
	global_store_dwordx2 v[0:1], v[54:55], off offset:32
	v_cvt_pk_f16_f32 v55, v80, v81
	v_cvt_pk_f16_f32 v54, v78, v79
	v_cmp_gt_u32_e64 s[4:5], 32, v103
	global_store_dwordx2 v[0:1], v[54:55], off offset:64
	v_cvt_pk_f16_f32 v55, v60, v61
	v_cvt_pk_f16_f32 v54, v58, v59
	global_store_dwordx2 v[0:1], v[54:55], off offset:96
	s_and_saveexec_b64 s[8:9], s[4:5]
	s_cbranch_execz .LBB0_13
	v_cvt_pk_f16_f32 v55, v84, v85
	v_cvt_pk_f16_f32 v54, v82, v83
	global_store_dwordx2 v[0:1], v[54:55], off offset:128

.LBB0_22:
	s_or_b64 exec, exec, s[4:5]
	s_waitcnt vmcnt(2)
	v_cvt_pk_f16_f32 v1, v12, v13
	v_cvt_pk_f16_f32 v0, v10, v11
	ds_write_b64 v90, v[0:1] offset:57600
	s_waitcnt vmcnt(1)
	v_cvt_pk_f16_f32 v1, v8, v9
	v_cvt_pk_f16_f32 v0, v6, v7
	ds_write_b64 v89, v[0:1] offset:57600
	s_and_saveexec_b64 s[0:1], s[2:3]
	s_cbranch_execz .LBB0_24
	v_mul_u32_u24_e32 v6, 0xe39, v106
	s_movk_i32 s2, 0xffee
	v_mul_i32_i24_sdwa v7, v6, s2 dst_sel:DWORD dst_unused:UNUSED_PAD src0_sel:WORD_1 src1_sel:DWORD
	s_movk_i32 s2, 0xa0
	s_waitcnt vmcnt(0)
	v_cvt_pk_f16_f32 v0, v2, v3
	v_mul_u32_u24_sdwa v2, v6, s2 dst_sel:DWORD dst_unused:UNUSED_PAD src0_sel:WORD_1 src1_sel:DWORD
	v_add_lshl_u32 v3, v7, v106, 3
	v_cvt_pk_f16_f32 v1, v4, v5
	v_add3_u32 v2, 0, v2, v3
	ds_write_b64 v2, v[0:1] offset:57600

.LBB0_26:
	s_or_b64 exec, exec, s[2:3]
	v_or_b32_e32 v0, 2, v104
	s_movk_i32 s0, 0x2d00
	v_mad_u32_u24 v28, v0, s0, 0
	v_mul_u32_u24_e32 v0, 0x140, v0
	v_lshlrev_b32_e32 v1, 2, v93
	v_add_u32_e32 v30, v28, v88
	v_add3_u32 v29, s11, v0, v1
	v_add3_u32 v32, v28, v92, v88
	v_add_u32_e32 v33, v30, v92
	s_waitcnt vmcnt(0)
	ds_read_b128 v[0:3], v29
	ds_read_b64_tr_b16 v[4:5], v32
	ds_read_b64_tr_b16 v[6:7], v33 offset:2560
	v_mov_b32_e32 v62, v52
	ds_read_b64_tr_b16 v[8:9], v32 offset:32
	v_lshl_add_u32 v31, v91, 1, v28
	s_waitcnt lgkmcnt(1)
	v_mfma_f32_16x16x32_f16 v[4:7], v[4:7], v[62:65], v[0:3]
	ds_read_b64_tr_b16 v[10:11], v33 offset:2592
	ds_read_b64_tr_b16 v[12:13], v32 offset:5120
	ds_read_b64_tr_b16 v[14:15], v33 offset:7680
	v_add_u32_e32 v34, v31, v92
	ds_read_b64_tr_b16 v[0:1], v34 offset:10240
	v_mov_b32_e32 v2, 0
	v_mov_b32_e32 v3, v2
	s_waitcnt lgkmcnt(1)
	v_mfma_f32_16x16x32_f16 v[4:7], v[12:15], v[58:61], v[4:7]
	ds_read_b64_tr_b16 v[12:13], v34 offset:10272
	ds_read_b128 v[16:19], v29 offset:64
	v_mov_b32_e32 v14, v2
	s_waitcnt lgkmcnt(2)
	v_mfma_f32_16x16x32_f16 v[4:7], v[0:3], v[54:57], v[4:7]
	ds_read_b64_tr_b16 v[20:21], v32 offset:5152
	ds_read_b64_tr_b16 v[22:23], v33 offset:7712
	v_mov_b32_e32 v15, v2
	s_waitcnt lgkmcnt(2)
	v_mfma_f32_16x16x32_f16 v[8:11], v[8:11], v[62:65], v[16:19]
	ds_read_b64_tr_b16 v[24:25], v32 offset:64
	v_add3_u32 v28, v28, v95, v88
	v_add_u32_e32 v30, v30, v95
	ds_read_b128 v[16:19], v29 offset:128
	s_waitcnt lgkmcnt(2)
	v_mfma_f32_16x16x32_f16 v[8:11], v[20:23], v[58:61], v[8:11]
	ds_read_b64_tr_b16 v[26:27], v33 offset:2624
	ds_read_b64_tr_b16 v[20:21], v32 offset:5184
	s_movk_i32 s2, 0xa0
	v_mfma_f32_16x16x32_f16 v[8:11], v[12:15], v[54:57], v[8:11]
	ds_read_b64_tr_b16 v[22:23], v33 offset:7744
	ds_read_b64_tr_b16 v[0:1], v34 offset:10304
	v_mad_u32_u24 v35, v102, s2, v86
	s_waitcnt lgkmcnt(3)
	v_mfma_f32_16x16x32_f16 v[12:15], v[24:27], v[62:65], v[16:19]
	ds_read_b64_tr_b16 v[24:25], v28
	s_nop 1
	ds_read_b128 v[16:19], v29 offset:192
	v_add_u32_e32 v49, v35, v50
	s_waitcnt lgkmcnt(3)
	v_mfma_f32_16x16x32_f16 v[12:15], v[20:23], v[58:61], v[12:15]
	ds_read_b64_tr_b16 v[26:27], v30 offset:2560
	ds_read_b64_tr_b16 v[20:21], v28 offset:5120
	v_lshlrev_b32_e32 v48, 1, v87
	s_waitcnt lgkmcnt(4)
	v_mfma_f32_16x16x32_f16 v[12:15], v[0:3], v[54:57], v[12:15]
	ds_read_b64_tr_b16 v[22:23], v30 offset:7680
	v_add_u32_e32 v0, v31, v95
	ds_read_b64_tr_b16 v[0:1], v0 offset:10240
	s_waitcnt lgkmcnt(3)
	v_mfma_f32_16x16x32_f16 v[16:19], v[24:27], v[62:65], v[16:19]
	ds_read_b128 v[24:27], v29 offset:256
	ds_read_b64_tr_b16 v[28:29], v32 offset:128
	v_add_u32_e32 v36, v35, v48
	s_waitcnt lgkmcnt(3)
	v_mfma_f32_16x16x32_f16 v[16:19], v[20:23], v[58:61], v[16:19]
	ds_read_b64_tr_b16 v[30:31], v33 offset:2688
	ds_read_b64_tr_b16 v[20:21], v32 offset:5248
	v_add_u32_e32 v32, 0xb000, v49
	s_waitcnt lgkmcnt(4)
	v_mfma_f32_16x16x32_f16 v[16:19], v[0:3], v[54:57], v[16:19]
	ds_read_b64_tr_b16 v[22:23], v33 offset:7808
	ds_read_b64_tr_b16 v[0:1], v34 offset:10368
	v_add_u32_e32 v44, 0x80, v36
	s_waitcnt lgkmcnt(3)
	v_mfma_f32_16x16x32_f16 v[24:27], v[28:31], v[62:65], v[24:27]
	ds_read2_b64 v[28:31], v32 offset0:128 offset1:132
	ds_read2_b64 v[32:35], v32 offset0:136 offset1:140
	v_add_u32_e32 v40, 0xb800, v49
	s_waitcnt lgkmcnt(3)
	v_mfma_f32_16x16x32_f16 v[20:23], v[20:23], v[58:61], v[24:27]
	ds_read2_b64 v[36:39], v40 offset0:192 offset1:196
	v_cmp_gt_u32_e64 s[0:1], 32, v103
	v_cvt_pk_f16_f32 v11, v10, v11
	ds_read2st64_b64 v[24:27], v44 offset0:90 offset1:95
	s_waitcnt lgkmcnt(4)
	v_mfma_f32_16x16x32_f16 v[20:23], v[0:3], v[54:57], v[20:23]
	v_cvt_pk_f16_f32 v10, v8, v9
	v_cvt_pk_f16_f32 v9, v6, v7
	v_cvt_pk_f16_f32 v8, v4, v5
	ds_read2_b64 v[4:7], v40 offset0:200 offset1:204
	v_cvt_pk_f16_f32 v19, v18, v19
	s_nop 2
	v_cvt_pk_f16_f32 v0, v22, v23
	v_cvt_pk_f16_f32 v1, v20, v21
	v_cndmask_b32_e64 v21, 0, v0, s[0:1]
	v_add_u32_e32 v0, 0xc800, v49
	ds_read2_b64 v[40:43], v0 offset1:4
	s_waitcnt lgkmcnt(5)
	v_mfma_f32_16x16x32_f16 v[28:31], v[28:31], v[8:11], 0
	v_cndmask_b32_e64 v20, 0, v1, s[0:1]
	v_cvt_pk_f16_f32 v18, v16, v17
	v_cvt_pk_f16_f32 v17, v14, v15
	v_cvt_pk_f16_f32 v16, v12, v13
	ds_read2_b64 v[12:15], v0 offset0:8 offset1:12
	s_waitcnt lgkmcnt(3)
	v_mov_b32_e32 v0, v24
	v_mov_b32_e32 v1, v25
	ds_read2st64_b64 v[44:47], v44 offset0:100 offset1:105
	v_mfma_f32_16x16x32_f16 v[28:31], v[32:35], v[16:19], v[28:31]
	v_mov_b32_e32 v22, v2
	v_mov_b32_e32 v23, v2
	v_add_u32_e32 v24, 0xd000, v49
	ds_read2_b64 v[32:35], v24 offset0:64 offset1:68
	ds_read2_b64 v[52:55], v24 offset0:72 offset1:76
	v_mfma_f32_16x16x32_f16 v[28:31], v[0:3], v[20:23], v[28:31]
	v_or_b32_e32 v0, 64, v102
	v_min_u32_e32 v0, 0x47, v0
	v_mad_u32_u24 v49, v0, s2, v86
	v_add_u32_e32 v0, v49, v50
	v_add_u32_e32 v0, 0xb000, v0
	ds_read2_b64 v[56:59], v0 offset0:128 offset1:132
	ds_read2_b64 v[60:63], v0 offset0:136 offset1:140
	v_mfma_f32_16x16x32_f16 v[36:39], v[36:39], v[8:11], 0
	v_mov_b32_e32 v0, v26
	v_mov_b32_e32 v1, v27
	s_movk_i32 s2, 0x48
	s_waitcnt lgkmcnt(7)
	v_mfma_f32_16x16x32_f16 v[4:7], v[4:7], v[16:19], v[36:39]
	v_mov_b32_e32 v51, v2
	v_mfma_f32_16x16x32_f16 v[24:27], v[0:3], v[20:23], v[4:7]
	s_waitcnt lgkmcnt(4)
	v_mov_b32_e32 v0, v44
	v_mov_b32_e32 v1, v45
	v_mfma_f32_16x16x32_f16 v[4:7], v[40:43], v[8:11], 0
	v_mfma_f32_16x16x32_f16 v[4:7], v[12:15], v[16:19], v[4:7]
	v_mfma_f32_16x16x32_f16 v[12:15], v[0:3], v[20:23], v[4:7]
	v_mov_b32_e32 v0, v46
	v_mov_b32_e32 v1, v47
	s_waitcnt lgkmcnt(3)
	v_mfma_f32_16x16x32_f16 v[4:7], v[32:35], v[8:11], 0
	s_waitcnt lgkmcnt(2)
	v_mfma_f32_16x16x32_f16 v[4:7], v[52:55], v[16:19], v[4:7]
	v_mfma_f32_16x16x32_f16 v[32:35], v[0:3], v[20:23], v[4:7]
	v_add_u32_e32 v0, v49, v48
	ds_read_b64 v[0:1], v0 offset:46208
	s_waitcnt lgkmcnt(2)
	v_mfma_f32_16x16x32_f16 v[4:7], v[56:59], v[8:11], 0
	v_mul_lo_u32 v8, v97, s2
	s_mov_b32 s2, 0x3e2e1a92
	v_ashrrev_i32_e32 v9, 31, v8
	s_waitcnt lgkmcnt(1)
	v_mfma_f32_16x16x32_f16 v[4:7], v[60:63], v[16:19], v[4:7]
	s_waitcnt lgkmcnt(0)
	v_mfma_f32_16x16x32_f16 v[4:7], v[0:3], v[20:23], v[4:7]
	v_mov_b32_e32 v0, s63
	v_mov_b32_e32 v1, s61
	v_cndmask_b32_e32 v1, v0, v1, vcc
	v_mov_b32_e32 v0, s62
	v_mov_b32_e32 v3, s60
	v_cndmask_b32_e32 v0, v0, v3, vcc
	v_mov_b32_e32 v2, v29
	v_mov_b32_e32 v3, v30
	v_pk_mul_f32 v[2:3], v[2:3], s[2:3] op_sel_hi:[1,0]
	v_lshl_add_u64 v[0:1], v[8:9], 1, v[0:1]
	v_fma_mixlo_f16 v8, v28, s2, 0
	v_cvt_pk_f16_f32 v3, v2, v3
	v_pack_b32_f16 v2, v8, v3
	v_fma_mixlo_f16 v8, v31, s2, 0
	v_lshl_add_u64 v[0:1], v[0:1], 0, v[50:51]
	v_alignbit_b32 v3, v8, v3, 16
	global_store_dwordx2 v[0:1], v[2:3], off
	v_mov_b32_e32 v2, v25
	v_mov_b32_e32 v3, v26
	v_pk_mul_f32 v[2:3], v[2:3], s[2:3] op_sel_hi:[1,0]
	v_fma_mixlo_f16 v8, v24, s2, 0
	v_cvt_pk_f16_f32 v3, v2, v3
	v_pack_b32_f16 v2, v8, v3
	v_fma_mixlo_f16 v8, v27, s2, 0
	v_alignbit_b32 v3, v8, v3, 16
	global_store_dwordx2 v[0:1], v[2:3], off offset:32
	v_mov_b32_e32 v2, v13
	v_mov_b32_e32 v3, v14
	v_pk_mul_f32 v[2:3], v[2:3], s[2:3] op_sel_hi:[1,0]
	v_fma_mixlo_f16 v8, v12, s2, 0
	v_cvt_pk_f16_f32 v3, v2, v3
	v_pack_b32_f16 v2, v8, v3
	v_fma_mixlo_f16 v8, v15, s2, 0
	v_alignbit_b32 v3, v8, v3, 16
	global_store_dwordx2 v[0:1], v[2:3], off offset:64
	v_mov_b32_e32 v2, v33
	v_mov_b32_e32 v3, v34
	v_pk_mul_f32 v[2:3], v[2:3], s[2:3] op_sel_hi:[1,0]
	v_fma_mixlo_f16 v8, v32, s2, 0
	v_cvt_pk_f16_f32 v3, v2, v3
	v_pack_b32_f16 v2, v8, v3
	v_fma_mixlo_f16 v8, v35, s2, 0
	v_alignbit_b32 v3, v8, v3, 16
	global_store_dwordx2 v[0:1], v[2:3], off offset:96
	s_and_saveexec_b64 s[4:5], s[0:1]
	s_cbranch_execz .LBB0_28
	v_mov_b32_e32 v2, v5
	v_mov_b32_e32 v3, v6
	v_pk_mul_f32 v[2:3], v[2:3], s[2:3] op_sel_hi:[1,0]
	v_fma_mixlo_f16 v4, v4, s2, 0
	v_cvt_pk_f16_f32 v3, v2, v3
	v_pack_b32_f16 v2, v4, v3
	v_fma_mixlo_f16 v4, v7, s2, 0
	v_alignbit_b32 v3, v4, v3, 16
	global_store_dwordx2 v[0:1], v[2:3], off offset:128
.LBB0_28:
	s_endpgm
	.p2align	8

	.amdhsa_kernel _Z7k_pointPDF16_S_S_PKfS1_S1_S1_S1_S1_S1_S1_S1_S1_S1_S1_S1_S1_
		.amdhsa_group_segment_fixed_size 0
		.amdhsa_private_segment_fixed_size 0
		.amdhsa_kernarg_size 136
		.amdhsa_user_sgpr_count 2
		.amdhsa_user_sgpr_dispatch_ptr 0
		.amdhsa_user_sgpr_queue_ptr 0
		.amdhsa_user_sgpr_kernarg_segment_ptr 1
		.amdhsa_user_sgpr_dispatch_id 0
		.amdhsa_user_sgpr_kernarg_preload_length 0
		.amdhsa_user_sgpr_kernarg_preload_offset 0
		.amdhsa_user_sgpr_private_segment_size 0
		.amdhsa_uses_dynamic_stack 0
		.amdhsa_enable_private_segment 0
		.amdhsa_system_sgpr_workgroup_id_x 1
		.amdhsa_system_sgpr_workgroup_id_y 0
		.amdhsa_system_sgpr_workgroup_id_z 0
		.amdhsa_system_sgpr_workgroup_info 0
		.amdhsa_system_vgpr_workitem_id 0
		.amdhsa_next_free_vgpr 169
		.amdhsa_next_free_sgpr 96
		.amdhsa_accum_offset 160
		.amdhsa_reserve_vcc 1
		.amdhsa_float_round_mode_32 0
		.amdhsa_float_round_mode_16_64 0
		.amdhsa_float_denorm_mode_32 3
		.amdhsa_float_denorm_mode_16_64 3
		.amdhsa_dx10_clamp 1
		.amdhsa_ieee_mode 1
		.amdhsa_fp16_overflow 0
		.amdhsa_tg_split 0
		.amdhsa_exception_fp_ieee_invalid_op 0
		.amdhsa_exception_fp_denorm_src 0
		.amdhsa_exception_fp_ieee_div_zero 0
		.amdhsa_exception_fp_ieee_overflow 0
		.amdhsa_exception_fp_ieee_underflow 0
		.amdhsa_exception_fp_ieee_inexact 0
		.amdhsa_exception_int_div_zero 0
	.end_amdhsa_kernel

.LBB1_26:
	v_lshlrev_b32_e32 v28, 1, v20
	v_add3_u32 v24, 0, v28, v21
	v_add_u32_e32 v22, v22, v28
	ds_read_b64_tr_b16 v[10:11], v24 offset:57664
	ds_read_b64_tr_b16 v[12:13], v22 offset:60224
	ds_read_b128 v[18:21], v26 offset:128
	ds_read_b64_tr_b16 v[26:27], v22 offset:65344
	ds_read_b64_tr_b16 v[24:25], v24 offset:62784
	v_add_u32_e32 v22, v23, v28
	ds_read_b64_tr_b16 v[28:29], v22 offset:10304
	s_waitcnt lgkmcnt(3)
	v_mfma_f32_16x16x32_f16 v[6:9], v[10:13], v[6:9], v[18:21]
	v_mov_b32_e32 v30, 0
	v_mov_b32_e32 v31, v30
	s_waitcnt lgkmcnt(1)
	v_mfma_f32_16x16x32_f16 v[6:9], v[24:27], v[14:17], v[6:9]
	s_waitcnt lgkmcnt(0)
	v_mfma_f32_16x16x32_f16 v[0:3], v[28:31], v[0:3], v[6:9]
	s_nop 7
	v_cvt_pk_f16_f32 v3, v2, v3
	v_cvt_pk_f16_f32 v2, v0, v1
	global_store_dwordx2 v[4:5], v[2:3], off offset:64
	s_endpgm
	.p2align	8
